# P0 x rmsnorm/quantise loop: next trip's 8 row loads issued a trip ahead into a second register set (software prefetch), loop-invariant gate-bias load hoisted
# baseline (speedup 1.0000x reference)
; #define GAS __attribute__((address_space(1)))
; __device__ __forceinline__ void p0_prologue(Frame& F, const Args& A) {
;     ...
;     {
;         const float* x = A.in[0]; const float* gmix = A.in[2]; const float* bg = A.in[4];
;         unsigned char* xn = ws + WS_R1; float* rsc = (float*)(ws + WS_SA); float* gates = (float*)(ws + WS_GATES);
;         f32x4 g[4]; float gacc = 0.f;
; #pragma unroll
;         for (int j = 0; j < 4; ++j) g[j] = *(const f32x4*)(gmix + 4 * lane + 256 * j);
; #pragma unroll 1
;         for (int repx = 0; repx < P0X_REP; ++repx)
;         for (int m0 = gw, trip = 0; m0 < T; m0 += 2 * NGW) {
;             f32x4 vv[2][4];
; #pragma unroll
;             for (int rr = 0; rr < 2; ++rr) { const int m = m0 + rr * NGW; const GAS f32x4* xr = (const GAS f32x4*)(x + (size_t)(m < T ? m : m0) * D) + lane;
; #pragma unroll
;                 for (int j = 0; j < 4; ++j) vv[rr][j] = xr[64 * j]; }
.LBB0_29:
	s_or_b64 exec, exec, s[2:3]
	v_lshlrev_b32_e32 v146, 2, v196
	s_cmp_lt_i32 s14, 0x10000
	v_mov_b32_e32 v163, 0
	v_and_b32_e32 v197, 7, v198
	v_cmp_eq_u32_e64 s[2:3], 0, v196
	v_lshlrev_b32_e32 v1, 2, v146
	v_lshlrev_b32_e32 v162, 2, v167
	s_cbranch_scc0 .LBB0_48
	global_load_dwordx4 v[2:5], v1, s[20:21]
	global_load_dwordx4 v[6:9], v1, s[20:21] offset:1024
	global_load_dwordx4 v[10:13], v1, s[20:21] offset:2048
	global_load_dwordx4 v[14:17], v1, s[20:21] offset:3072
	v_and_b32_e32 v18, 32, v198
	v_cmp_eq_u32_e64 s[4:5], 0, v18
	v_and_b32_e32 v18, 16, v198
	v_cmp_eq_u32_e64 s[6:7], 0, v18
	v_and_b32_e32 v18, 8, v198
	v_cmp_eq_u32_e64 s[8:9], 0, v18
	v_and_b32_e32 v18, 1, v198
	v_mov_b32_e32 v19, s34
	v_cmp_eq_u32_e32 vcc, 1, v18
	s_mov_b64 s[12:13], 0x3000000
	v_lshl_add_u32 v142, v196, 4, 0
	v_cndmask_b32_e32 v18, 0, v19, vcc
	v_add_u32_e32 v166, s14, v18
	v_lshl_add_u64 v[18:19], s[58:59], 0, v[162:163]
	v_lshl_add_u64 v[170:171], v[18:19], 0, s[12:13]
	v_mbcnt_lo_u32_b32 v18, -1, 0
	v_mbcnt_hi_u32_b32 v18, -1, v18
	v_and_b32_e32 v20, 64, v18
	v_xor_b32_e32 v19, 32, v18
	v_add_u32_e32 v20, 64, v20
	v_cmp_lt_i32_e32 vcc, v19, v20
	v_mov_b32_e32 v147, v163
	s_add_u32 s35, s58, 0x4600000
	v_cndmask_b32_e32 v19, v18, v19, vcc
	v_lshlrev_b32_e32 v200, 2, v19
	v_xor_b32_e32 v19, 16, v18
	v_cmp_lt_i32_e32 vcc, v19, v20
	v_mov_b32_e32 v165, v163
	v_lshl_add_u64 v[146:147], s[58:59], 0, v[146:147]
	v_cndmask_b32_e32 v19, v18, v19, vcc
	v_lshlrev_b32_e32 v201, 2, v19
	v_xor_b32_e32 v19, 8, v18
	v_cmp_lt_i32_e32 vcc, v19, v20
	s_mov_b64 s[12:13], 0x15000000
	s_mov_b32 s15, 0
	v_cndmask_b32_e32 v18, v18, v19, vcc
	v_lshlrev_b32_e32 v202, 2, v18
	ds_read_b128 v[18:21], v142
	ds_read_b128 v[22:25], v142 offset:1024
	ds_read_b128 v[26:29], v142 offset:2048
	ds_read_b128 v[30:33], v142 offset:3072
	ds_read_b128 v[34:37], v142 offset:4096
	ds_read_b128 v[38:41], v142 offset:5120
	ds_read_b128 v[42:45], v142 offset:6144
	ds_read_b128 v[46:49], v142 offset:7168
	ds_read_b128 v[50:53], v142 offset:8192
	ds_read_b128 v[54:57], v142 offset:9216
	ds_read_b128 v[58:61], v142 offset:10240
	ds_read_b128 v[62:65], v142 offset:11264
	ds_read_b128 v[66:69], v142 offset:12288
	ds_read_b128 v[70:73], v142 offset:13312
	ds_read_b128 v[74:77], v142 offset:14336
	ds_read_b128 v[78:81], v142 offset:15360
	ds_read_b128 v[82:85], v142 offset:16384
	ds_read_b128 v[86:89], v142 offset:17408
	ds_read_b128 v[90:93], v142 offset:18432
	ds_read_b128 v[94:97], v142 offset:19456
	ds_read_b128 v[98:101], v142 offset:20480
	ds_read_b128 v[102:105], v142 offset:21504
	ds_read_b128 v[106:109], v142 offset:22528
	ds_read_b128 v[110:113], v142 offset:23552
	ds_read_b128 v[114:117], v142 offset:24576
	ds_read_b128 v[118:121], v142 offset:25600
	ds_read_b128 v[122:125], v142 offset:26624
	ds_read_b128 v[126:129], v142 offset:27648
	ds_read_b128 v[130:133], v142 offset:28672
	ds_read_b128 v[134:137], v142 offset:29696
	ds_read_b128 v[138:141], v142 offset:30720
	ds_read_b128 v[142:145], v142 offset:31744
	v_bfe_u32 v199, v198, 1, 2
	v_lshl_add_u64 v[168:169], s[24:25], 0, v[162:163]
	v_cmp_lt_u32_e64 s[10:11], 31, v196
	s_addc_u32 s70, s59, 0
	s_lshl_b32 s71, s92, 4
	v_lshl_add_u64 v[172:173], s[16:17], 0, v[164:165]
	v_lshl_add_u64 v[174:175], v[146:147], 0, s[12:13]
	v_mov_b32_e32 v165, 0x358637bd
	s_mov_b32 s72, 0x800000
	s_mov_b32 s73, 0x42fe0000
	s_mov_b32 s74, 0xc0c0400
	s_mov_b32 s75, 0x5040100
	v_mov_b32_e32 v203, 0x3ca908c9
	v_mov_b32_e32 v204, 0x3ecc95a3
	v_mov_b32_e32 v205, 0x7f800000
	v_mov_b32_e32 v176, 0x3f317218
	v_mov_b32_e32 v206, 0
	s_mov_b32 s20, s14
	s_mov_b32 s94, 0
	global_load_dword v250, v[168:169], off
	s_mov_b32 s99, 0
	s_mov_b32 s98, s20
	s_lshl_b64 s[100:101], s[98:99], 12
	v_lshl_add_u64 v[248:249], v[172:173], 0, s[100:101]
	global_load_dwordx4 v[216:219], v[248:249], off nt
	global_load_dwordx4 v[220:223], v[248:249], off offset:1024 nt
	global_load_dwordx4 v[224:227], v[248:249], off offset:2048 nt
	global_load_dwordx4 v[228:231], v[248:249], off offset:3072 nt
	s_add_i32 s100, s98, s34
	s_cmp_lt_i32 s100, 0x10000
	s_cselect_b32 s98, s100, s98
	s_lshl_b64 s[100:101], s[98:99], 12
	v_lshl_add_u64 v[248:249], v[172:173], 0, s[100:101]
	global_load_dwordx4 v[232:235], v[248:249], off nt
	global_load_dwordx4 v[236:239], v[248:249], off offset:1024 nt
	global_load_dwordx4 v[240:243], v[248:249], off offset:2048 nt
	global_load_dwordx4 v[244:247], v[248:249], off offset:3072 nt
	s_branch .LBB0_34

; #define GAS __attribute__((address_space(1)))
; __device__ __forceinline__ void p0_prologue(Frame& F, const Args& A) {
;     ...
;         for (int m0 = gw, trip = 0; m0 < T; m0 += 2 * NGW) {
;             f32x4 vv[2][4];
; #pragma unroll
;             for (int rr = 0; rr < 2; ++rr) { const int m = m0 + rr * NGW; const GAS f32x4* xr = (const GAS f32x4*)(x + (size_t)(m < T ? m : m0) * D) + lane;
; #pragma unroll
;                 for (int j = 0; j < 4; ++j) vv[rr][j] = xr[64 * j]; }
; #pragma unroll
;             for (int rr = 0; rr < 2; ++rr) { const int mraw = m0 + rr * NGW; const bool mvalid = mraw < T; const int m = mvalid ? mraw : m0;
;                 f32x4 v[4]; float s = 0.f;
; #pragma unroll
;                 for (int j = 0; j < 4; ++j) { v[j] = vv[rr][j]; s += (v[j].x * v[j].x + v[j].y * v[j].y) + (v[j].z * v[j].z + v[j].w * v[j].w); }
;                 const float r = rsqrtf(wave_sum(s) * (1.f / D) + EPS);
; #pragma unroll
;                 for (int j = 0; j < 4; ++j) v[j] = v[j] * r * g[j];
.LBB0_34:
	s_waitcnt vmcnt(0)
	v_mov_b64_e32 v[178:179], v[216:217]
	v_mov_b64_e32 v[180:181], v[218:219]
	v_mov_b64_e32 v[182:183], v[220:221]
	v_mov_b64_e32 v[184:185], v[222:223]
	v_mov_b64_e32 v[208:209], v[224:225]
	v_mov_b64_e32 v[210:211], v[226:227]
	v_mov_b64_e32 v[212:213], v[228:229]
	v_mov_b64_e32 v[214:215], v[230:231]
	v_mov_b64_e32 v[158:159], v[232:233]
	v_mov_b64_e32 v[160:161], v[234:235]
	v_mov_b64_e32 v[154:155], v[236:237]
	v_mov_b64_e32 v[156:157], v[238:239]
	v_mov_b64_e32 v[150:151], v[240:241]
	v_mov_b64_e32 v[152:153], v[242:243]
	v_mov_b64_e32 v[146:147], v[244:245]
	v_mov_b64_e32 v[148:149], v[246:247]
	s_ashr_i32 s21, s20, 31
	s_lshl_b64 s[12:13], s[20:21], 12
	s_add_i32 s95, s20, s34
	s_cmp_lt_i32 s95, 0x10000
	s_cselect_b64 s[66:67], -1, 0
	s_and_b64 s[12:13], s[66:67], exec
	s_cselect_b32 s24, s95, s20
	s_ashr_i32 s25, s24, 31
	s_lshl_b64 s[12:13], s[24:25], 12
	s_add_i32 s98, s95, s34
	s_cmp_gt_i32 s98, 0xffff
	s_cbranch_scc1 .Lmy_p0x_nopf
	s_mov_b32 s99, 0
	s_lshl_b64 s[100:101], s[98:99], 12
	v_lshl_add_u64 v[248:249], v[172:173], 0, s[100:101]
	global_load_dwordx4 v[216:219], v[248:249], off nt
	global_load_dwordx4 v[220:223], v[248:249], off offset:1024 nt
	global_load_dwordx4 v[224:227], v[248:249], off offset:2048 nt
	global_load_dwordx4 v[228:231], v[248:249], off offset:3072 nt
	s_add_i32 s100, s98, s34
	s_cmp_lt_i32 s100, 0x10000
	s_cselect_b32 s98, s100, s98
	s_lshl_b64 s[100:101], s[98:99], 12
	v_lshl_add_u64 v[248:249], v[172:173], 0, s[100:101]
	global_load_dwordx4 v[232:235], v[248:249], off nt
	global_load_dwordx4 v[236:239], v[248:249], off offset:1024 nt
	global_load_dwordx4 v[240:243], v[248:249], off offset:2048 nt
	global_load_dwordx4 v[244:247], v[248:249], off offset:3072 nt
.Lmy_p0x_nopf:
	v_pk_mul_f32 v[186:187], v[180:181], v[180:181]
	v_pk_mul_f32 v[188:189], v[178:179], v[178:179]
	v_mul_f32_e32 v177, v212, v212
	v_pk_mov_b32 v[190:191], v[188:189], v[186:187] op_sel:[1,0]
	v_mov_b32_e32 v189, v187
	v_pk_add_f32 v[186:187], v[190:191], v[188:189]
	v_pk_mul_f32 v[188:189], v[184:185], v[184:185]
	v_pk_mul_f32 v[190:191], v[182:183], v[182:183]
	v_pk_add_f32 v[186:187], v[186:187], v[186:187] op_sel:[0,1] op_sel_hi:[1,0]
	v_pk_mov_b32 v[192:193], v[190:191], v[188:189] op_sel:[1,0]
	v_mov_b32_e32 v191, v189
	v_pk_add_f32 v[188:189], v[192:193], v[190:191]
	v_mul_f32_e32 v190, v213, v213
	v_pk_add_f32 v[188:189], v[188:189], v[188:189] op_sel:[0,1] op_sel_hi:[1,0]
	v_mov_b32_e32 v187, v177
	v_mov_b32_e32 v189, v190
	v_pk_add_f32 v[186:187], v[186:187], v[188:189]
	v_mul_f32_e32 v188, v209, v209
	v_mul_f32_e32 v191, v214, v214
	v_pk_fma_f32 v[188:189], v[208:209], v[208:209], v[188:189] op_sel_hi:[1,1,0]
	v_mul_f32_e32 v190, v211, v211
	v_mul_f32_e32 v192, v215, v215
	v_mov_b32_e32 v189, v191
	v_pk_fma_f32 v[190:191], v[210:211], v[210:211], v[190:191] op_sel_hi:[1,1,0]
	s_nop 0
	v_mov_b32_e32 v191, v192
	v_pk_add_f32 v[188:189], v[188:189], v[190:191]
	s_nop 0
	v_pk_add_f32 v[186:187], v[186:187], v[188:189]
	s_nop 0
	v_add_f32_e32 v177, v186, v187
	s_nop 1
	v_add_f32_dpp v177, v177, v177 row_ror:1 row_mask:0xf bank_mask:0xf bound_ctrl:1
	s_nop 1
	v_add_f32_dpp v177, v177, v177 row_ror:2 row_mask:0xf bank_mask:0xf bound_ctrl:1
	s_nop 1
	v_add_f32_dpp v177, v177, v177 row_ror:4 row_mask:0xf bank_mask:0xf bound_ctrl:1
	s_nop 1
	v_add_f32_dpp v177, v177, v177 row_ror:8 row_mask:0xf bank_mask:0xf bound_ctrl:1
	s_nop 0
	v_readlane_b32 vcc_lo, v177, 16
	v_readlane_b32 vcc_hi, v177, 48
	v_readlane_b32 s12, v177, 0
	v_readlane_b32 s13, v177, 32
	v_mov_b32_e32 v186, vcc_lo
	v_mov_b32_e32 v187, vcc_hi
	v_pk_add_f32 v[186:187], s[12:13], v[186:187]
	s_nop 0
	v_add_f32_e32 v177, v186, v187
	v_fmamk_f32 v177, v177, 0x3a800000, v165
	v_cmp_gt_f32_e32 vcc, s72, v177
	v_mul_f32_e32 v186, 0x4b800000, v177
	s_nop 0
	v_cndmask_b32_e32 v177, v177, v186, vcc
	v_rsq_f32_e32 v177, v177
	s_nop 0
	v_mul_f32_e32 v186, 0x45800000, v177
	v_cndmask_b32_e32 v194, v177, v186, vcc
	v_pk_mul_f32 v[178:179], v[178:179], v[194:195] op_sel_hi:[1,0]
	v_pk_mul_f32 v[180:181], v[180:181], v[194:195] op_sel_hi:[1,0]
	v_pk_mul_f32 v[192:193], v[2:3], v[178:179]
	v_pk_mul_f32 v[178:179], v[182:183], v[194:195] op_sel_hi:[1,0]
	v_pk_mul_f32 v[188:189], v[4:5], v[180:181]
	v_pk_mul_f32 v[180:181], v[184:185], v[194:195] op_sel_hi:[1,0]
	v_pk_mul_f32 v[190:191], v[6:7], v[178:179]
	v_pk_mul_f32 v[178:179], v[208:209], v[194:195] op_sel_hi:[1,0]
	v_pk_mul_f32 v[184:185], v[8:9], v[180:181]
	v_pk_mul_f32 v[180:181], v[210:211], v[194:195] op_sel_hi:[1,0]
	v_pk_mul_f32 v[186:187], v[10:11], v[178:179]
	v_pk_mul_f32 v[182:183], v[212:213], v[194:195] op_sel_hi:[1,0]
	v_pk_mul_f32 v[178:179], v[214:215], v[194:195] op_sel_hi:[1,0]
	v_max_f32_e64 v177, |v192|, |v193|
	v_max_f32_e64 v194, |v188|, |v189|
	v_pk_mul_f32 v[180:181], v[12:13], v[180:181]
	v_max3_f32 v177, v177, 0, v194
	v_max_f32_e64 v194, |v190|, |v191|
	v_max_f32_e64 v195, |v184|, |v185|
	v_pk_mul_f32 v[178:179], v[16:17], v[178:179]
	v_pk_mul_f32 v[182:183], v[14:15], v[182:183]
	v_max3_f32 v177, v177, v194, v195
	v_max_f32_e64 v194, |v186|, |v187|
	v_max_f32_e64 v195, |v180|, |v181|
	v_max3_f32 v177, v177, v194, v195
	v_max_f32_e64 v194, |v182|, |v183|
	v_max_f32_e64 v195, |v178|, |v179|
	v_max3_f32 v177, v177, v194, v195
	v_mov_b32_e32 v194, 0
	s_nop 1
	v_mov_b32_dpp v194, v177 row_ror:1 row_mask:0xf bank_mask:0xf
	v_max_f32_e32 v194, v194, v194
	v_max_f32_e32 v177, v177, v194
	v_mov_b32_e32 v194, 0
	s_nop 1
	v_mov_b32_dpp v194, v177 row_ror:2 row_mask:0xf bank_mask:0xf
	v_max_f32_e32 v194, v194, v194
	v_max_f32_e32 v177, v177, v194
	v_mov_b32_e32 v194, 0
	s_nop 1
; #define GAS __attribute__((address_space(1)))
; #define LAS __attribute__((address_space(3)))
; __device__ __forceinline__ void p0_prologue(Frame& F, const Args& A) {
;     ...
;                 { float mx = 0.f;
; #pragma unroll
;                   for (int j = 0; j < 4; ++j) mx = fmaxf(fmaxf(mx, fmaxf(fabsf(v[j].x), fabsf(v[j].y))), fmaxf(fabsf(v[j].z), fabsf(v[j].w)));
;                   mx = wave_max(mx); const float qs = mx > 0.f ? 127.0f / mx : 0.f;
;                   GAS unsigned* o4 = (GAS unsigned*)(xn + (size_t)m * D) + lane;
;                   if (mvalid) {
; #pragma unroll
;                   for (int j = 0; j < 4; ++j) o4[64 * j] = pk4_i8s(v[j].x, v[j].y, v[j].z, v[j].w, qs);
;                   if (lane == 0) rsc[m] = mx * (1.0f / 127.0f); } }
;                 float gs[8];
; #pragma unroll
;                 for (int jg = 0; jg < 8; ++jg) { float a = 0.f;
; #pragma unroll
;                     for (int j = 0; j < 4; ++j) { const f32x4 w = *(const LAS f32x4*)(wgs + jg * D + 4 * lane + 256 * j); a += (v[j].x * w.x + v[j].y * w.y) + (v[j].z * w.z + v[j].w * w.w); }
;                     gs[jg] = a; }
	v_mov_b32_dpp v194, v177 row_ror:4 row_mask:0xf bank_mask:0xf
	v_max_f32_e32 v194, v194, v194
	v_max_f32_e32 v177, v177, v194
	v_mov_b32_e32 v194, 0
	s_nop 1
	v_mov_b32_dpp v194, v177 row_ror:8 row_mask:0xf bank_mask:0xf
	v_max_f32_e32 v194, v194, v194
	v_max_f32_e32 v177, v177, v194
	s_nop 0
	v_readlane_b32 vcc_lo, v177, 32
	v_readlane_b32 vcc_hi, v177, 48
	v_readlane_b32 s12, v177, 0
	v_readlane_b32 s13, v177, 16
	v_max_f32_e64 v177, vcc_hi, vcc_hi
	v_max_f32_e64 v194, vcc_lo, vcc_lo
	v_max_f32_e32 v177, v194, v177
	v_mov_b32_e32 v194, s13
	v_max3_f32 v177, s12, v194, v177
	v_div_scale_f32 v207, vcc, v177, v177, s73
	v_rcp_f32_e32 v208, v207
	s_lshl_b64 s[12:13], s[20:21], 10
	v_lshl_add_u64 v[194:195], v[174:175], 0, s[12:13]
	v_cmp_lt_f32_e64 s[12:13], 0, v177
	v_fma_f32 v209, -v207, v208, 1.0
	v_fmac_f32_e32 v208, v209, v208
	v_div_scale_f32 v209, vcc, s73, v177, s73
	v_mul_f32_e32 v210, v209, v208
	v_fma_f32 v211, -v207, v210, v209
	v_fmac_f32_e32 v210, v211, v208
	v_fma_f32 v207, -v207, v210, v209
	v_div_fmas_f32 v207, v207, v208, v210
	v_div_fixup_f32 v207, v207, v177, s73
	v_cndmask_b32_e64 v207, 0, v207, s[12:13]
	v_fmaak_f32 v208, v192, v207, 0x4b400000
	v_fmaak_f32 v209, v193, v207, 0x4b400000
	v_fmaak_f32 v210, v188, v207, 0x4b400000
	v_fmaak_f32 v211, v189, v207, 0x4b400000
	v_perm_b32 v210, v211, v210, s74
	v_perm_b32 v208, v209, v208, s74
	v_perm_b32 v208, v210, v208, s75
	global_store_dword v[194:195], v208, off
	v_fmaak_f32 v208, v190, v207, 0x4b400000
	v_fmaak_f32 v209, v191, v207, 0x4b400000
	v_fmaak_f32 v210, v184, v207, 0x4b400000
	v_fmaak_f32 v211, v185, v207, 0x4b400000
	v_perm_b32 v210, v211, v210, s74
	v_perm_b32 v208, v209, v208, s74
	v_perm_b32 v208, v210, v208, s75
	global_store_dword v[194:195], v208, off offset:256
	v_fmaak_f32 v208, v186, v207, 0x4b400000
	v_fmaak_f32 v209, v187, v207, 0x4b400000
	v_fmaak_f32 v210, v180, v207, 0x4b400000
	v_fmaak_f32 v211, v181, v207, 0x4b400000
	v_perm_b32 v210, v211, v210, s74
	v_perm_b32 v208, v209, v208, s74
	v_perm_b32 v208, v210, v208, s75
	global_store_dword v[194:195], v208, off offset:512
	v_fmaak_f32 v208, v182, v207, 0x4b400000
	v_fmaak_f32 v209, v183, v207, 0x4b400000
	v_fmaak_f32 v210, v178, v207, 0x4b400000
	v_fmaak_f32 v207, v179, v207, 0x4b400000
	v_perm_b32 v207, v207, v210, s74
	v_perm_b32 v208, v209, v208, s74
	v_perm_b32 v207, v207, v208, s75
	global_store_dword v[194:195], v207, off offset:768
	s_and_saveexec_b64 s[12:13], s[2:3]
	s_cbranch_execz .LBB0_36
	s_lshl_b64 vcc, s[20:21], 2
	s_add_u32 vcc_lo, s35, vcc_lo
	v_mul_f32_e32 v177, 0x3c010204, v177
	s_addc_u32 vcc_hi, s70, vcc_hi
	global_store_dword v163, v177, vcc
.LBB0_36:
	s_or_b64 exec, exec, s[12:13]
	s_waitcnt lgkmcnt(14)
	v_mul_f32_e32 v177, v193, v19
	v_mul_f32_e32 v194, v189, v21
	v_fmac_f32_e32 v177, v192, v18
	v_fmac_f32_e32 v194, v188, v20
	v_add_f32_e32 v177, v177, v194
	v_mul_f32_e32 v194, v191, v23
	v_mul_f32_e32 v195, v185, v25
	v_fmac_f32_e32 v194, v190, v22
	v_fmac_f32_e32 v195, v184, v24
	v_add_f32_e32 v177, 0, v177
	v_add_f32_e32 v194, v194, v195
	v_add_f32_e32 v177, v177, v194
	v_mul_f32_e32 v194, v187, v27
	v_mul_f32_e32 v195, v181, v29
	v_fmac_f32_e32 v194, v186, v26
	v_fmac_f32_e32 v195, v180, v28
	v_add_f32_e32 v194, v194, v195
	v_add_f32_e32 v177, v177, v194
	v_mul_f32_e32 v194, v183, v31
	v_mul_f32_e32 v195, v179, v33
	v_fmac_f32_e32 v194, v182, v30
	v_fmac_f32_e32 v195, v178, v32
	v_add_f32_e32 v194, v194, v195
	v_add_f32_e32 v177, v177, v194
	v_mul_f32_e32 v194, v193, v35
	v_mul_f32_e32 v195, v189, v37
	v_fmac_f32_e32 v194, v192, v34
	v_fmac_f32_e32 v195, v188, v36
	v_add_f32_e32 v194, v194, v195
	v_mul_f32_e32 v195, v191, v39
	v_mul_f32_e32 v207, v185, v41
	v_fmac_f32_e32 v195, v190, v38
	v_fmac_f32_e32 v207, v184, v40
	v_add_f32_e32 v194, 0, v194
	v_add_f32_e32 v195, v195, v207
	v_add_f32_e32 v194, v194, v195
	v_mul_f32_e32 v195, v187, v43
	v_mul_f32_e32 v207, v181, v45
	v_fmac_f32_e32 v195, v186, v42
	v_fmac_f32_e32 v207, v180, v44
	v_add_f32_e32 v195, v195, v207
	v_add_f32_e32 v194, v194, v195
	v_mul_f32_e32 v195, v183, v47
	v_mul_f32_e32 v207, v179, v49
	v_fmac_f32_e32 v195, v182, v46
	v_fmac_f32_e32 v207, v178, v48
	v_add_f32_e32 v195, v195, v207
	v_add_f32_e32 v194, v194, v195
	v_mul_f32_e32 v195, v193, v51
	v_mul_f32_e32 v207, v189, v53
	v_fmac_f32_e32 v195, v192, v50
	v_fmac_f32_e32 v207, v188, v52
	v_add_f32_e32 v195, v195, v207
	v_mul_f32_e32 v207, v191, v55
	v_mul_f32_e32 v208, v185, v57
	v_fmac_f32_e32 v207, v190, v54
	v_fmac_f32_e32 v208, v184, v56
	v_add_f32_e32 v195, 0, v195
	v_add_f32_e32 v207, v207, v208
	v_add_f32_e32 v195, v195, v207
	v_mul_f32_e32 v207, v187, v59
	v_mul_f32_e32 v208, v181, v61
	v_fmac_f32_e32 v207, v186, v58
	v_fmac_f32_e32 v208, v180, v60
	v_add_f32_e32 v207, v207, v208
	v_add_f32_e32 v195, v195, v207
	v_mul_f32_e32 v207, v183, v63
	v_mul_f32_e32 v208, v179, v65
	v_fmac_f32_e32 v207, v182, v62
	v_fmac_f32_e32 v208, v178, v64
	v_add_f32_e32 v207, v207, v208
	v_add_f32_e32 v195, v195, v207
	v_mul_f32_e32 v207, v193, v67
	v_mul_f32_e32 v208, v189, v69
	v_fmac_f32_e32 v207, v192, v66
	v_fmac_f32_e32 v208, v188, v68
	v_add_f32_e32 v207, v207, v208
	v_mul_f32_e32 v208, v191, v71
	v_mul_f32_e32 v209, v185, v73
	v_fmac_f32_e32 v208, v190, v70
	v_fmac_f32_e32 v209, v184, v72
	v_add_f32_e32 v207, 0, v207
	v_add_f32_e32 v208, v208, v209
	v_add_f32_e32 v207, v207, v208
	v_mul_f32_e32 v208, v187, v75
	v_mul_f32_e32 v209, v181, v77
	v_fmac_f32_e32 v208, v186, v74
	v_fmac_f32_e32 v209, v180, v76
	v_add_f32_e32 v208, v208, v209
	v_add_f32_e32 v207, v207, v208
	v_mul_f32_e32 v208, v183, v79
	v_mul_f32_e32 v209, v179, v81
	v_fmac_f32_e32 v208, v182, v78
	v_fmac_f32_e32 v209, v178, v80
	v_add_f32_e32 v208, v208, v209
	v_add_f32_e32 v207, v207, v208
	v_mul_f32_e32 v208, v193, v83
	v_mul_f32_e32 v209, v189, v85
	v_fmac_f32_e32 v208, v192, v82
	v_fmac_f32_e32 v209, v188, v84
	v_add_f32_e32 v208, v208, v209
	v_mul_f32_e32 v209, v191, v87
	v_mul_f32_e32 v210, v185, v89
	v_fmac_f32_e32 v209, v190, v86
	v_fmac_f32_e32 v210, v184, v88
	v_add_f32_e32 v208, 0, v208
	v_add_f32_e32 v209, v209, v210
	v_add_f32_e32 v208, v208, v209
	s_waitcnt lgkmcnt(13)
; #define LAS __attribute__((address_space(3)))
; __device__ __forceinline__ void p0_prologue(Frame& F, const Args& A) {
;     ...
;                 for (int jg = 0; jg < 8; ++jg) { float a = 0.f;
; #pragma unroll
;                     for (int j = 0; j < 4; ++j) { const f32x4 w = *(const LAS f32x4*)(wgs + jg * D + 4 * lane + 256 * j); a += (v[j].x * w.x + v[j].y * w.y) + (v[j].z * w.z + v[j].w * w.w); }
;                     gs[jg] = a; }
;                 float g4[4], g2[2], g1;
;                 { const bool hi = (lane & 32) != 0;
; #pragma unroll
;                   for (int q = 0; q < 4; ++q) { const float keep = hi ? gs[4 + q] : gs[q], send = hi ? gs[q] : gs[4 + q]; g4[q] = keep + __shfl_xor(send, 32); } }
;                 { const bool hi = (lane & 16) != 0;
; #pragma unroll
;                   for (int q = 0; q < 2; ++q) { const float keep = hi ? g4[2 + q] : g4[q], send = hi ? g4[q] : g4[2 + q]; g2[q] = keep + __shfl_xor(send, 16); } }
;                 { const bool hi = (lane & 8) != 0; const float keep = hi ? g2[1] : g2[0], send = hi ? g2[0] : g2[1]; g1 = keep + __shfl_xor(send, 8); }
;                 g1 = sum8(g1);
	v_mul_f32_e32 v209, v187, v91
	v_mul_f32_e32 v210, v181, v93
	v_fmac_f32_e32 v209, v186, v90
	v_fmac_f32_e32 v210, v180, v92
	v_add_f32_e32 v209, v209, v210
	v_add_f32_e32 v208, v208, v209
	s_waitcnt lgkmcnt(12)
	v_mul_f32_e32 v209, v183, v95
	v_mul_f32_e32 v210, v179, v97
	v_fmac_f32_e32 v209, v182, v94
	v_fmac_f32_e32 v210, v178, v96
	v_add_f32_e32 v209, v209, v210
	v_add_f32_e32 v208, v208, v209
	s_waitcnt lgkmcnt(11)
	v_mul_f32_e32 v209, v193, v99
	v_mul_f32_e32 v210, v189, v101
	v_fmac_f32_e32 v209, v192, v98
	v_fmac_f32_e32 v210, v188, v100
	v_add_f32_e32 v209, v209, v210
	s_waitcnt lgkmcnt(10)
	v_mul_f32_e32 v210, v191, v103
	v_mul_f32_e32 v211, v185, v105
	v_fmac_f32_e32 v210, v190, v102
	v_fmac_f32_e32 v211, v184, v104
	v_add_f32_e32 v209, 0, v209
	v_add_f32_e32 v210, v210, v211
	v_add_f32_e32 v209, v209, v210
	s_waitcnt lgkmcnt(9)
	v_mul_f32_e32 v210, v187, v107
	v_mul_f32_e32 v211, v181, v109
	v_fmac_f32_e32 v210, v186, v106
	v_fmac_f32_e32 v211, v180, v108
	v_add_f32_e32 v210, v210, v211
	v_add_f32_e32 v209, v209, v210
	s_waitcnt lgkmcnt(8)
	v_mul_f32_e32 v210, v183, v111
	v_mul_f32_e32 v211, v179, v113
	v_fmac_f32_e32 v210, v182, v110
	v_fmac_f32_e32 v211, v178, v112
	v_add_f32_e32 v210, v210, v211
	v_add_f32_e32 v209, v209, v210
	s_waitcnt lgkmcnt(7)
	v_mul_f32_e32 v210, v193, v115
	v_mul_f32_e32 v211, v189, v117
	v_fmac_f32_e32 v210, v192, v114
	v_fmac_f32_e32 v211, v188, v116
	v_add_f32_e32 v210, v210, v211
	s_waitcnt lgkmcnt(6)
	v_mul_f32_e32 v211, v191, v119
	v_mul_f32_e32 v212, v185, v121
	s_waitcnt lgkmcnt(3)
	v_mul_f32_e32 v193, v193, v131
	v_mul_f32_e32 v189, v189, v133
	v_fmac_f32_e32 v211, v190, v118
	v_fmac_f32_e32 v212, v184, v120
	v_fmac_f32_e32 v193, v192, v130
	v_fmac_f32_e32 v189, v188, v132
	v_add_f32_e32 v210, 0, v210
	v_add_f32_e32 v211, v211, v212
	v_add_f32_e32 v188, v193, v189
	s_waitcnt lgkmcnt(2)
	v_mul_f32_e32 v189, v191, v135
	v_mul_f32_e32 v185, v185, v137
	v_add_f32_e32 v210, v210, v211
	v_mul_f32_e32 v211, v187, v123
	v_mul_f32_e32 v212, v181, v125
	v_fmac_f32_e32 v189, v190, v134
	v_fmac_f32_e32 v185, v184, v136
	v_fmac_f32_e32 v211, v186, v122
	v_fmac_f32_e32 v212, v180, v124
	v_add_f32_e32 v184, v189, v185
	s_waitcnt lgkmcnt(1)
	v_mul_f32_e32 v185, v187, v139
	v_mul_f32_e32 v181, v181, v141
	v_add_f32_e32 v211, v211, v212
	v_fmac_f32_e32 v185, v186, v138
	v_fmac_f32_e32 v181, v180, v140
	v_add_f32_e32 v210, v210, v211
	v_mul_f32_e32 v211, v183, v127
	v_add_f32_e32 v180, v185, v181
	s_waitcnt lgkmcnt(0)
	v_mul_f32_e32 v181, v183, v143
	v_fmac_f32_e32 v211, v182, v126
	v_fmac_f32_e32 v181, v182, v142
	v_cndmask_b32_e64 v182, v177, v208, s[4:5]
	ds_bpermute_b32 v182, v200, v182
	v_mul_f32_e32 v212, v179, v129
	v_add_f32_e32 v188, 0, v188
	v_mul_f32_e32 v179, v179, v145
	v_fmac_f32_e32 v212, v178, v128
	v_add_f32_e32 v184, v188, v184
	v_fmac_f32_e32 v179, v178, v144
	v_add_f32_e32 v211, v211, v212
	v_add_f32_e32 v180, v184, v180
	v_add_f32_e32 v178, v181, v179
	v_add_f32_e32 v210, v210, v211
	v_add_f32_e32 v178, v180, v178
	v_cndmask_b32_e64 v177, v208, v177, s[4:5]
	v_cndmask_b32_e64 v180, v194, v209, s[4:5]
	s_waitcnt lgkmcnt(0)
	v_add_f32_e32 v177, v177, v182
	ds_bpermute_b32 v180, v200, v180
	v_cndmask_b32_e64 v181, v195, v210, s[4:5]
	v_cndmask_b32_e64 v182, v207, v178, s[4:5]
	ds_bpermute_b32 v181, v200, v181
	ds_bpermute_b32 v182, v200, v182
	v_cndmask_b32_e64 v179, v209, v194, s[4:5]
	s_waitcnt lgkmcnt(2)
	v_add_f32_e32 v179, v179, v180
	v_cndmask_b32_e64 v180, v210, v195, s[4:5]
	v_cndmask_b32_e64 v178, v178, v207, s[4:5]
	s_waitcnt lgkmcnt(1)
	v_add_f32_e32 v180, v180, v181
	s_waitcnt lgkmcnt(0)
	v_add_f32_e32 v178, v178, v182
	v_cndmask_b32_e64 v181, v177, v180, s[6:7]
	v_cndmask_b32_e64 v182, v179, v178, s[6:7]
	ds_bpermute_b32 v181, v201, v181
	ds_bpermute_b32 v182, v201, v182
	v_cndmask_b32_e64 v177, v180, v177, s[6:7]
	v_cndmask_b32_e64 v178, v178, v179, s[6:7]
	s_waitcnt lgkmcnt(1)
	v_add_f32_e32 v177, v177, v181
	s_waitcnt lgkmcnt(0)
	v_add_f32_e32 v178, v178, v182
	v_cndmask_b32_e64 v179, v177, v178, s[8:9]
	ds_bpermute_b32 v179, v202, v179
	v_cndmask_b32_e64 v177, v178, v177, s[8:9]
	v_pk_mul_f32 v[180:181], v[158:159], v[158:159]
	s_waitcnt lgkmcnt(0)
; #define GAS __attribute__((address_space(1)))
; __device__ __forceinline__ void p0_prologue(Frame& F, const Args& A) {
;     ...
;             for (int rr = 0; rr < 2; ++rr) { const int mraw = m0 + rr * NGW; const bool mvalid = mraw < T; const int m = mvalid ? mraw : m0;
;                 f32x4 v[4]; float s = 0.f;
; #pragma unroll
;                 for (int j = 0; j < 4; ++j) { v[j] = vv[rr][j]; s += (v[j].x * v[j].x + v[j].y * v[j].y) + (v[j].z * v[j].z + v[j].w * v[j].w); }
;                 const float r = rsqrtf(wave_sum(s) * (1.f / D) + EPS);
; #pragma unroll
;                 for (int j = 0; j < 4; ++j) v[j] = v[j] * r * g[j];
;                 { float mx = 0.f;
; #pragma unroll
;                   for (int j = 0; j < 4; ++j) mx = fmaxf(fmaxf(mx, fmaxf(fabsf(v[j].x), fabsf(v[j].y))), fmaxf(fabsf(v[j].z), fabsf(v[j].w)));
;                   mx = wave_max(mx); const float qs = mx > 0.f ? 127.0f / mx : 0.f;
;                   GAS unsigned* o4 = (GAS unsigned*)(xn + (size_t)m * D) + lane;
;                   if (mvalid) {
; #pragma unroll
;                   for (int j = 0; j < 4; ++j) o4[64 * j] = pk4_i8s(v[j].x, v[j].y, v[j].z, v[j].w, qs);
;                   if (lane == 0) rsc[m] = mx * (1.0f / 127.0f); } }
	v_add_f32_e32 v177, v177, v179
	v_pk_mul_f32 v[178:179], v[160:161], v[160:161]
	s_nop 0
	v_add_f32_dpp v177, v177, v177 quad_perm:[1,0,3,2] row_mask:0xf bank_mask:0xf bound_ctrl:1
	v_pk_mov_b32 v[182:183], v[180:181], v[178:179] op_sel:[1,0]
	v_mov_b32_e32 v181, v179
	v_pk_add_f32 v[178:179], v[182:183], v[180:181]
	v_pk_mul_f32 v[180:181], v[156:157], v[156:157]
	v_pk_mul_f32 v[182:183], v[154:155], v[154:155]
	v_pk_add_f32 v[178:179], v[178:179], v[178:179] op_sel:[0,1] op_sel_hi:[1,0]
	v_pk_mov_b32 v[184:185], v[182:183], v[180:181] op_sel:[1,0]
	v_mov_b32_e32 v183, v181
	v_pk_add_f32 v[180:181], v[184:185], v[182:183]
	v_mul_f32_e32 v182, v146, v146
	v_mul_f32_e32 v183, v147, v147
	v_pk_add_f32 v[180:181], v[180:181], v[180:181] op_sel:[0,1] op_sel_hi:[1,0]
	v_mov_b32_e32 v179, v182
	v_mov_b32_e32 v181, v183
	v_pk_add_f32 v[178:179], v[178:179], v[180:181]
	v_mul_f32_e32 v180, v151, v151
	v_mul_f32_e32 v182, v153, v153
	v_mul_f32_e32 v184, v148, v148
	v_mul_f32_e32 v185, v149, v149
	v_pk_fma_f32 v[180:181], v[150:151], v[150:151], v[180:181] op_sel_hi:[1,1,0]
	v_pk_fma_f32 v[182:183], v[152:153], v[152:153], v[182:183] op_sel_hi:[1,1,0]
	v_mov_b32_e32 v181, v184
	v_mov_b32_e32 v183, v185
	v_pk_add_f32 v[180:181], v[180:181], v[182:183]
	v_add_f32_dpp v177, v177, v177 quad_perm:[2,3,0,1] row_mask:0xf bank_mask:0xf bound_ctrl:1
	v_pk_add_f32 v[178:179], v[178:179], v[180:181]
	s_nop 0
	v_add_f32_e32 v178, v178, v179
	s_nop 1
	v_add_f32_dpp v178, v178, v178 row_ror:1 row_mask:0xf bank_mask:0xf bound_ctrl:1
	s_nop 1
	v_add_f32_dpp v178, v178, v178 row_ror:2 row_mask:0xf bank_mask:0xf bound_ctrl:1
	s_nop 1
	v_add_f32_dpp v178, v178, v178 row_ror:4 row_mask:0xf bank_mask:0xf bound_ctrl:1
	s_nop 1
	v_add_f32_dpp v178, v178, v178 row_ror:8 row_mask:0xf bank_mask:0xf bound_ctrl:1
	s_nop 0
	v_readlane_b32 s21, v178, 16
	v_readlane_b32 vcc_lo, v178, 48
	v_readlane_b32 s12, v178, 0
	v_readlane_b32 s13, v178, 32
	v_mov_b32_e32 v178, s21
	v_mov_b32_e32 v179, vcc_lo
	v_pk_add_f32 v[178:179], s[12:13], v[178:179]
	s_nop 0
	v_add_f32_e32 v178, v178, v179
	v_fmamk_f32 v178, v178, 0x3a800000, v165
	v_mul_f32_e32 v179, 0x4b800000, v178
	v_cmp_gt_f32_e32 vcc, s72, v178
	s_nop 1
	v_cndmask_b32_e32 v178, v178, v179, vcc
	v_rsq_f32_e32 v179, v178
	v_mov_b32_e32 v178, 0
	v_mul_f32_e32 v180, 0x45800000, v179
	v_cndmask_b32_e32 v180, v179, v180, vcc
	v_pk_mul_f32 v[182:183], v[158:159], v[180:181] op_sel_hi:[1,0]
	v_pk_mul_f32 v[158:159], v[160:161], v[180:181] op_sel_hi:[1,0]
	v_pk_mul_f32 v[160:161], v[2:3], v[182:183]
	v_pk_mul_f32 v[182:183], v[154:155], v[180:181] op_sel_hi:[1,0]
	v_pk_mul_f32 v[158:159], v[4:5], v[158:159]
	v_pk_mul_f32 v[154:155], v[156:157], v[180:181] op_sel_hi:[1,0]
	v_pk_mul_f32 v[156:157], v[6:7], v[182:183]
	v_pk_mul_f32 v[182:183], v[150:151], v[180:181] op_sel_hi:[1,0]
	v_pk_mul_f32 v[154:155], v[8:9], v[154:155]
	v_pk_mul_f32 v[150:151], v[152:153], v[180:181] op_sel_hi:[1,0]
	v_pk_mul_f32 v[152:153], v[10:11], v[182:183]
	v_pk_mul_f32 v[182:183], v[146:147], v[180:181] op_sel_hi:[1,0]
	v_pk_mul_f32 v[146:147], v[148:149], v[180:181] op_sel_hi:[1,0]
	v_max_f32_e64 v179, |v160|, |v161|
	v_max_f32_e64 v180, |v158|, |v159|
	v_pk_mul_f32 v[150:151], v[12:13], v[150:151]
	v_max3_f32 v179, v179, 0, v180
	v_max_f32_e64 v180, |v156|, |v157|
	v_max_f32_e64 v181, |v154|, |v155|
	v_pk_mul_f32 v[146:147], v[16:17], v[146:147]
	v_pk_mul_f32 v[148:149], v[14:15], v[182:183]
	v_max3_f32 v179, v179, v180, v181
	v_max_f32_e64 v180, |v152|, |v153|
	v_max_f32_e64 v181, |v150|, |v151|
	v_max3_f32 v179, v179, v180, v181
	v_max_f32_e64 v180, |v148|, |v149|
	v_max_f32_e64 v181, |v146|, |v147|
	v_max3_f32 v179, v179, v180, v181
	v_mov_b32_e32 v180, 0
	v_mov_b32_dpp v178, v177 row_half_mirror row_mask:0xf bank_mask:0xf
	s_andn2_b64 vcc, exec, s[66:67]
	v_mov_b32_dpp v180, v179 row_ror:1 row_mask:0xf bank_mask:0xf
	v_max_f32_e32 v180, v180, v180
	v_max_f32_e32 v179, v179, v180
	v_mov_b32_e32 v180, 0
	s_nop 1
	v_mov_b32_dpp v180, v179 row_ror:2 row_mask:0xf bank_mask:0xf
	v_max_f32_e32 v180, v180, v180
	v_max_f32_e32 v179, v179, v180
	v_mov_b32_e32 v180, 0
	s_nop 1
	v_mov_b32_dpp v180, v179 row_ror:4 row_mask:0xf bank_mask:0xf
	v_max_f32_e32 v180, v180, v180
	v_max_f32_e32 v179, v179, v180
	v_mov_b32_e32 v180, 0
	s_nop 1
	v_mov_b32_dpp v180, v179 row_ror:8 row_mask:0xf bank_mask:0xf
	v_max_f32_e32 v180, v180, v180
	v_max_f32_e32 v179, v179, v180
	s_nop 0
	v_readlane_b32 s12, v179, 0
	v_readlane_b32 s13, v179, 16
	v_readlane_b32 s21, v179, 32
	v_readlane_b32 s66, v179, 48
	s_cbranch_vccnz .LBB0_40
	s_nop 0
	v_max_f32_e64 v179, s66, s66
	v_max_f32_e64 v180, s21, s21
	v_max_f32_e32 v179, v180, v179
	v_mov_b32_e32 v180, s13
	v_max3_f32 v179, s12, v180, v179
	v_div_scale_f32 v182, s[12:13], v179, v179, s73
	v_rcp_f32_e32 v183, v182
	s_lshl_b64 s[12:13], s[24:25], 10
	v_lshl_add_u64 v[180:181], v[174:175], 0, s[12:13]
	v_fma_f32 v184, -v182, v183, 1.0
	v_fmac_f32_e32 v183, v184, v183
	v_div_scale_f32 v184, vcc, s73, v179, s73
	v_mul_f32_e32 v185, v184, v183
	v_fma_f32 v186, -v182, v185, v184
	v_fmac_f32_e32 v185, v186, v183
	v_fma_f32 v182, -v182, v185, v184
	v_div_fmas_f32 v182, v182, v183, v185
	v_div_fixup_f32 v182, v182, v179, s73
	v_cmp_lt_f32_e32 vcc, 0, v179
	s_nop 1
	v_cndmask_b32_e32 v182, 0, v182, vcc
	v_fmaak_f32 v183, v160, v182, 0x4b400000
	v_fmaak_f32 v184, v161, v182, 0x4b400000
	v_fmaak_f32 v185, v158, v182, 0x4b400000
	v_fmaak_f32 v186, v159, v182, 0x4b400000
	v_perm_b32 v185, v186, v185, s74
	v_perm_b32 v183, v184, v183, s74
	v_perm_b32 v183, v185, v183, s75
	global_store_dword v[180:181], v183, off
	v_fmaak_f32 v183, v156, v182, 0x4b400000
	v_fmaak_f32 v184, v157, v182, 0x4b400000
	v_fmaak_f32 v185, v154, v182, 0x4b400000
	v_fmaak_f32 v186, v155, v182, 0x4b400000
	v_perm_b32 v185, v186, v185, s74
	v_perm_b32 v183, v184, v183, s74
	v_perm_b32 v183, v185, v183, s75
	global_store_dword v[180:181], v183, off offset:256
	v_fmaak_f32 v183, v152, v182, 0x4b400000
	v_fmaak_f32 v184, v153, v182, 0x4b400000
	v_fmaak_f32 v185, v150, v182, 0x4b400000
	v_fmaak_f32 v186, v151, v182, 0x4b400000
	v_perm_b32 v185, v186, v185, s74
	v_perm_b32 v183, v184, v183, s74
	v_perm_b32 v183, v185, v183, s75
	global_store_dword v[180:181], v183, off offset:512
	v_fmaak_f32 v183, v148, v182, 0x4b400000
	v_fmaak_f32 v184, v149, v182, 0x4b400000
	v_fmaak_f32 v185, v146, v182, 0x4b400000
	v_fmaak_f32 v182, v147, v182, 0x4b400000
	v_perm_b32 v182, v182, v185, s74
	v_perm_b32 v183, v184, v183, s74
	v_perm_b32 v182, v182, v183, s75
	global_store_dword v[180:181], v182, off offset:768
	s_and_saveexec_b64 s[12:13], s[2:3]
	s_cbranch_execz .LBB0_39
	s_lshl_b64 s[24:25], s[24:25], 2
	s_add_u32 s24, s35, s24
	v_mul_f32_e32 v179, 0x3c010204, v179
	s_addc_u32 s25, s70, s25
	global_store_dword v163, v179, s[24:25]

; #define LAS __attribute__((address_space(3)))
; __device__ __forceinline__ void p0_prologue(Frame& F, const Args& A) {
;     ...
;                 float gs[8];
; #pragma unroll
;                 for (int jg = 0; jg < 8; ++jg) { float a = 0.f;
; #pragma unroll
;                     for (int j = 0; j < 4; ++j) { const f32x4 w = *(const LAS f32x4*)(wgs + jg * D + 4 * lane + 256 * j); a += (v[j].x * w.x + v[j].y * w.y) + (v[j].z * w.z + v[j].w * w.w); }
;                     gs[jg] = a; }
;                 float g4[4], g2[2], g1;
;                 { const bool hi = (lane & 32) != 0;
; #pragma unroll
;                   for (int q = 0; q < 4; ++q) { const float keep = hi ? gs[4 + q] : gs[q], send = hi ? gs[q] : gs[4 + q]; g4[q] = keep + __shfl_xor(send, 32); } }
.LBB0_40:
	v_add_f32_e32 v177, v177, v178
	v_mul_f32_e32 v178, v19, v161
	v_mul_f32_e32 v179, v21, v159
	v_fmac_f32_e32 v178, v18, v160
	v_fmac_f32_e32 v179, v20, v158
	v_add_f32_e32 v178, v178, v179
	v_mul_f32_e32 v179, v23, v157
	v_mul_f32_e32 v180, v25, v155
	v_fmac_f32_e32 v179, v22, v156
	v_fmac_f32_e32 v180, v24, v154
	v_add_f32_e32 v178, 0, v178
	v_add_f32_e32 v179, v179, v180
	v_add_f32_e32 v178, v179, v178
	v_mul_f32_e32 v179, v27, v153
	v_mul_f32_e32 v180, v29, v151
	v_fmac_f32_e32 v179, v26, v152
	v_fmac_f32_e32 v180, v28, v150
	v_add_f32_e32 v179, v179, v180
	v_add_f32_e32 v178, v179, v178
	v_mul_f32_e32 v179, v31, v149
	v_mul_f32_e32 v180, v33, v147
	v_fmac_f32_e32 v179, v30, v148
	v_fmac_f32_e32 v180, v32, v146
	v_add_f32_e32 v179, v179, v180
	v_add_f32_e32 v178, v179, v178
	v_mul_f32_e32 v179, v35, v161
	v_mul_f32_e32 v180, v37, v159
	v_fmac_f32_e32 v179, v34, v160
	v_fmac_f32_e32 v180, v36, v158
	v_add_f32_e32 v179, v179, v180
	v_mul_f32_e32 v180, v39, v157
	v_mul_f32_e32 v181, v41, v155
	v_fmac_f32_e32 v180, v38, v156
	v_fmac_f32_e32 v181, v40, v154
	v_add_f32_e32 v179, 0, v179
	v_add_f32_e32 v180, v180, v181
	v_add_f32_e32 v179, v180, v179
	v_mul_f32_e32 v180, v43, v153
	v_mul_f32_e32 v181, v45, v151
	v_fmac_f32_e32 v180, v42, v152
	v_fmac_f32_e32 v181, v44, v150
	v_add_f32_e32 v180, v180, v181
	v_add_f32_e32 v179, v180, v179
	v_mul_f32_e32 v180, v47, v149
	v_mul_f32_e32 v181, v49, v147
	v_fmac_f32_e32 v180, v46, v148
	v_fmac_f32_e32 v181, v48, v146
	v_add_f32_e32 v180, v180, v181
	v_add_f32_e32 v179, v180, v179
	v_mul_f32_e32 v180, v51, v161
	v_mul_f32_e32 v181, v53, v159
	v_fmac_f32_e32 v180, v50, v160
	v_fmac_f32_e32 v181, v52, v158
	v_add_f32_e32 v180, v180, v181
	v_mul_f32_e32 v181, v55, v157
	v_mul_f32_e32 v182, v57, v155
	v_fmac_f32_e32 v181, v54, v156
	v_fmac_f32_e32 v182, v56, v154
	v_add_f32_e32 v180, 0, v180
	v_add_f32_e32 v181, v181, v182
	v_add_f32_e32 v180, v181, v180
	v_mul_f32_e32 v181, v59, v153
	v_mul_f32_e32 v182, v61, v151
	v_fmac_f32_e32 v181, v58, v152
	v_fmac_f32_e32 v182, v60, v150
	v_add_f32_e32 v181, v181, v182
	v_add_f32_e32 v180, v181, v180
	v_mul_f32_e32 v181, v63, v149
	v_mul_f32_e32 v182, v65, v147
	v_fmac_f32_e32 v181, v62, v148
	v_fmac_f32_e32 v182, v64, v146
	v_add_f32_e32 v181, v181, v182
	v_add_f32_e32 v180, v181, v180
	v_mul_f32_e32 v181, v67, v161
	v_mul_f32_e32 v182, v69, v159
	v_fmac_f32_e32 v181, v66, v160
	v_fmac_f32_e32 v182, v68, v158
	v_add_f32_e32 v181, v181, v182
	v_mul_f32_e32 v182, v71, v157
	v_mul_f32_e32 v183, v73, v155
	v_fmac_f32_e32 v182, v70, v156
	v_fmac_f32_e32 v183, v72, v154
	v_add_f32_e32 v181, 0, v181
	v_add_f32_e32 v182, v182, v183
	v_add_f32_e32 v181, v182, v181
	v_mul_f32_e32 v182, v75, v153
	v_mul_f32_e32 v183, v77, v151
	v_fmac_f32_e32 v182, v74, v152
	v_fmac_f32_e32 v183, v76, v150
	v_add_f32_e32 v182, v182, v183
	v_add_f32_e32 v181, v182, v181
	v_mul_f32_e32 v182, v79, v149
	v_mul_f32_e32 v183, v81, v147
	v_fmac_f32_e32 v182, v78, v148
	v_fmac_f32_e32 v183, v80, v146
	v_add_f32_e32 v182, v182, v183
	v_add_f32_e32 v181, v182, v181
	v_mul_f32_e32 v182, v83, v161
	v_mul_f32_e32 v183, v85, v159
	v_fmac_f32_e32 v182, v82, v160
	v_fmac_f32_e32 v183, v84, v158
	v_add_f32_e32 v182, v182, v183
	v_mul_f32_e32 v183, v87, v157
	v_mul_f32_e32 v184, v89, v155
	v_fmac_f32_e32 v183, v86, v156
	v_fmac_f32_e32 v184, v88, v154
	v_add_f32_e32 v182, 0, v182
	v_add_f32_e32 v183, v183, v184
	v_add_f32_e32 v182, v183, v182
	v_mul_f32_e32 v183, v91, v153
	v_mul_f32_e32 v184, v93, v151
	v_fmac_f32_e32 v183, v90, v152
	v_fmac_f32_e32 v184, v92, v150
	v_add_f32_e32 v183, v183, v184
	v_add_f32_e32 v182, v183, v182
	v_mul_f32_e32 v183, v95, v149
	v_mul_f32_e32 v184, v97, v147
	v_fmac_f32_e32 v183, v94, v148
	v_fmac_f32_e32 v184, v96, v146
	v_add_f32_e32 v183, v183, v184
	v_add_f32_e32 v182, v183, v182
	v_mul_f32_e32 v183, v99, v161
	v_mul_f32_e32 v184, v101, v159
	v_fmac_f32_e32 v183, v98, v160
	v_fmac_f32_e32 v184, v100, v158
	v_add_f32_e32 v183, v183, v184
	v_mul_f32_e32 v184, v103, v157
	v_mul_f32_e32 v185, v105, v155
	v_fmac_f32_e32 v184, v102, v156
	v_fmac_f32_e32 v185, v104, v154
	v_add_f32_e32 v183, 0, v183
	v_add_f32_e32 v184, v184, v185
	v_add_f32_e32 v183, v184, v183
	v_mul_f32_e32 v184, v107, v153
	v_mul_f32_e32 v185, v109, v151
	v_fmac_f32_e32 v184, v106, v152
	v_fmac_f32_e32 v185, v108, v150
	v_add_f32_e32 v184, v184, v185
	v_add_f32_e32 v183, v184, v183
	v_mul_f32_e32 v184, v111, v149
	v_mul_f32_e32 v185, v113, v147
	v_fmac_f32_e32 v184, v110, v148
	v_fmac_f32_e32 v185, v112, v146
	v_add_f32_e32 v184, v184, v185
	v_add_f32_e32 v183, v184, v183
	v_mul_f32_e32 v184, v115, v161
	v_mul_f32_e32 v185, v117, v159
	v_fmac_f32_e32 v184, v114, v160
	v_fmac_f32_e32 v185, v116, v158
	v_add_f32_e32 v184, v184, v185
	v_mul_f32_e32 v185, v119, v157
	v_mul_f32_e32 v186, v121, v155
	v_fmac_f32_e32 v185, v118, v156
	v_fmac_f32_e32 v186, v120, v154
	v_add_f32_e32 v184, 0, v184
	v_add_f32_e32 v185, v185, v186
	v_add_f32_e32 v184, v185, v184
	v_mul_f32_e32 v185, v123, v153
	v_mul_f32_e32 v186, v125, v151
	v_fmac_f32_e32 v185, v122, v152
	v_fmac_f32_e32 v186, v124, v150
	v_mul_f32_e32 v161, v131, v161
	v_mul_f32_e32 v159, v133, v159
	v_add_f32_e32 v185, v185, v186
	v_fmac_f32_e32 v161, v130, v160
	v_fmac_f32_e32 v159, v132, v158
	v_mul_f32_e32 v157, v135, v157
	v_mul_f32_e32 v155, v137, v155
	v_add_f32_e32 v184, v185, v184
	v_mul_f32_e32 v185, v127, v149
	v_mul_f32_e32 v186, v129, v147
	v_add_f32_e32 v158, v161, v159
	v_fmac_f32_e32 v157, v134, v156
	v_fmac_f32_e32 v155, v136, v154
	v_mul_f32_e32 v153, v139, v153
	v_mul_f32_e32 v151, v141, v151
	v_fmac_f32_e32 v185, v126, v148
	v_fmac_f32_e32 v186, v128, v146
	v_add_f32_e32 v158, 0, v158
	v_add_f32_e32 v154, v157, v155
	v_fmac_f32_e32 v153, v138, v152
	v_fmac_f32_e32 v151, v140, v150
	v_mul_f32_e32 v149, v143, v149
	v_mul_f32_e32 v147, v145, v147
	v_add_f32_e32 v185, v185, v186
	v_add_f32_e32 v154, v154, v158
	v_add_f32_e32 v150, v153, v151
	v_fmac_f32_e32 v149, v142, v148
	v_fmac_f32_e32 v147, v144, v146
	v_cndmask_b32_e64 v148, v178, v182, s[4:5]
	v_add_f32_e32 v184, v185, v184
	v_add_f32_e32 v150, v150, v154
	v_add_f32_e32 v146, v149, v147
	ds_bpermute_b32 v148, v200, v148
	v_cndmask_b32_e64 v149, v179, v183, s[4:5]
	v_add_f32_e32 v146, v146, v150
	ds_bpermute_b32 v149, v200, v149
	v_cndmask_b32_e64 v150, v180, v184, s[4:5]
	ds_bpermute_b32 v150, v200, v150
	v_cndmask_b32_e64 v147, v182, v178, s[4:5]
	s_waitcnt lgkmcnt(2)
; __device__ __forceinline__ void p0_prologue(Frame& F, const Args& A) {
;     ...
;                   for (int q = 0; q < 4; ++q) { const float keep = hi ? gs[4 + q] : gs[q], send = hi ? gs[q] : gs[4 + q]; g4[q] = keep + __shfl_xor(send, 32); } }
;                 { const bool hi = (lane & 16) != 0;
; #pragma unroll
;                   for (int q = 0; q < 2; ++q) { const float keep = hi ? g4[2 + q] : g4[q], send = hi ? g4[q] : g4[2 + q]; g2[q] = keep + __shfl_xor(send, 16); } }
;                 { const bool hi = (lane & 8) != 0; const float keep = hi ? g2[1] : g2[0], send = hi ? g2[0] : g2[1]; g1 = keep + __shfl_xor(send, 8); }
;                 g1 = sum8(g1);
;                 if ((lane & 7) == 2 * (trip & 3) + rr) gacc = g1;
;             }
;             if ((trip & 3) == 3 || m0 + 2 * NGW >= T) { const int jg = lane >> 3, sub = lane & 7, tr = (trip & ~3) + (sub >> 1); const int m = gw + tr * 2 * NGW + (sub & 1) * NGW;
;                 if (tr <= trip && m < T) { const float pre = gacc + bg[jg];
;                     const float sc = 15.0f * tanhf(pre * (1.0f / 15.0f));
	v_add_f32_e32 v147, v147, v148
	v_cndmask_b32_e64 v148, v183, v179, s[4:5]
	s_waitcnt lgkmcnt(1)
	v_add_f32_e32 v148, v148, v149
	v_cndmask_b32_e64 v149, v184, v180, s[4:5]
	s_waitcnt lgkmcnt(0)
	v_add_f32_e32 v149, v149, v150
	v_cndmask_b32_e64 v150, v146, v181, s[4:5]
	v_cndmask_b32_e64 v146, v181, v146, s[4:5]
	ds_bpermute_b32 v146, v200, v146
	s_and_b32 s12, s15, 6
	v_cmp_eq_u32_e32 vcc, s12, v197
	s_or_b32 s12, s12, 1
	s_waitcnt lgkmcnt(0)
	v_add_f32_e32 v146, v150, v146
	v_cndmask_b32_e64 v150, v149, v147, s[6:7]
	v_cndmask_b32_e64 v147, v147, v149, s[6:7]
	v_cndmask_b32_e64 v149, v146, v148, s[6:7]
	v_cndmask_b32_e64 v146, v148, v146, s[6:7]
	ds_bpermute_b32 v147, v201, v147
	ds_bpermute_b32 v146, v201, v146
	v_cndmask_b32_e32 v177, v206, v177, vcc
	v_cmp_eq_u32_e32 vcc, s12, v197
	s_and_b32 s12, s94, 3
	s_waitcnt lgkmcnt(1)
	v_add_f32_e32 v147, v150, v147
	s_waitcnt lgkmcnt(0)
	v_add_f32_e32 v146, v149, v146
	v_cndmask_b32_e64 v148, v146, v147, s[8:9]
	v_cndmask_b32_e64 v146, v147, v146, s[8:9]
	ds_bpermute_b32 v146, v202, v146
	s_cmp_eq_u32 s12, 3
	s_cselect_b64 s[12:13], -1, 0
	s_add_i32 s20, s71, s20
	s_cmp_gt_i32 s20, 0xffff
	s_waitcnt lgkmcnt(0)
	v_add_f32_e32 v146, v148, v146
	s_cselect_b64 s[20:21], -1, 0
	s_or_b64 s[12:13], s[12:13], s[20:21]
	v_add_f32_dpp v146, v146, v146 quad_perm:[1,0,3,2] row_mask:0xf bank_mask:0xf bound_ctrl:1
	s_nop 1
	v_add_f32_dpp v146, v146, v146 quad_perm:[2,3,0,1] row_mask:0xf bank_mask:0xf bound_ctrl:1
	s_nop 1
	v_add_f32_dpp v146, v146, v146 row_half_mirror row_mask:0xf bank_mask:0xf bound_ctrl:1
	v_cndmask_b32_e32 v206, v177, v146, vcc
	s_andn2_b64 vcc, exec, s[12:13]
	s_cbranch_vccnz .LBB0_33
	s_and_b32 s12, s94, 0x7ffffffc
	v_or_b32_e32 v148, s12, v199
	v_mad_u64_u32 v[146:147], s[12:13], v148, s71, v[166:167]
	s_mov_b32 s12, 0x10000
	v_cmp_ge_u32_e32 vcc, s94, v148
	v_cmp_gt_i32_e64 s[12:13], s12, v146
	s_and_b64 s[20:21], vcc, s[12:13]
	s_and_saveexec_b64 s[12:13], s[20:21]
	s_cbranch_execz .LBB0_32
	v_mov_b32_e32 v147, v250
	s_mov_b32 s20, 0x3f200000
	v_add_f32_e32 v147, v206, v147
	v_mul_f32_e32 v147, 0x3d888889, v147
	v_cmp_nlt_f32_e64 s[20:21], |v147|, s20
	s_and_saveexec_b64 s[24:25], s[20:21]
	s_xor_b64 s[20:21], exec, s[24:25]
	s_cbranch_execz .LBB0_44
	v_add_f32_e64 v148, |v147|, |v147|
	v_mul_f32_e32 v149, 0x3fb8aa3b, v148
	v_rndne_f32_e32 v150, v149
	s_mov_b32 s24, 0x3fb8aa3b
	v_sub_f32_e32 v151, v149, v150
	v_fma_f32 v149, v148, s24, -v149
	v_fmac_f32_e32 v149, 0x32a5705f, v148
	v_add_f32_e32 v149, v151, v149
	v_cvt_i32_f32_e32 v150, v150
	v_exp_f32_e32 v149, v149
	s_mov_b32 s24, 0xc2ce8ed0
	v_cmp_ngt_f32_e32 vcc, s24, v148
	s_mov_b32 s24, 0x42b17218
	v_ldexp_f32 v149, v149, v150
	v_cndmask_b32_e32 v149, 0, v149, vcc
	v_cmp_nlt_f32_e32 vcc, s24, v148
	s_nop 1
	v_cndmask_b32_e32 v148, v205, v149, vcc
	v_add_f32_e32 v148, 1.0, v148
	v_rcp_f32_e32 v148, v148
	s_nop 0
	v_fma_f32 v148, v148, -2.0, 1.0

; __device__ __forceinline__ void p0_prologue(Frame& F, const Args& A) {
;     ...
;     {
;         const float* x = A.in[1]; const float* gmem = A.in[12]; unsigned char* mn = ws + WS_R3;
;         f32x4 g[4];
; #pragma unroll
;         for (int j = 0; j < 4; ++j) g[j] = *(const f32x4*)(gmem + 4 * lane + 256 * j);
;         for (int m = gw; m < TM; m += NGW) {
.LBB0_48:
	s_waitcnt vmcnt(0)
	s_cmpk_gt_i32 s14, 0x1fff
	s_cbranch_scc1 .LBB0_53
	global_load_dwordx4 v[2:5], v1, s[44:45]
	global_load_dwordx4 v[6:9], v1, s[44:45] offset:1024
	global_load_dwordx4 v[10:13], v1, s[44:45] offset:2048
	global_load_dwordx4 v[14:17], v1, s[44:45] offset:3072
	s_ashr_i32 s15, s14, 31
	s_lshl_b64 s[4:5], s[14:15], 2
	s_add_u32 s12, s4, 0x4680000
	s_addc_u32 s13, s5, 0
	s_ashr_i32 s35, s34, 31
	s_lshl_b64 s[6:7], s[14:15], 10
	s_lshl_b64 s[4:5], s[34:35], 2
	v_lshl_or_b32 v18, v196, 2, s6
	v_mov_b32_e32 v19, s7
	s_lshl_b64 s[6:7], s[34:35], 10
	s_lshl_b64 s[8:9], s[14:15], 12
	s_add_u32 s8, s18, s8
	v_mov_b32_e32 v165, 0
	s_addc_u32 s9, s19, s9
	v_lshl_add_u64 v[20:21], s[8:9], 0, v[164:165]
	s_mov_b64 s[8:9], 0xc00
	v_lshl_add_u64 v[20:21], v[20:21], 0, s[8:9]
	s_lshl_b64 s[8:9], s[34:35], 12
	v_mov_b32_e32 v1, 0x358637bd
	s_mov_b32 s15, 0x800000
	s_mov_b32 s18, 0x42fe0000
	s_mov_b32 s19, 0xc0c0400
	s_mov_b32 s20, 0x5040100
	s_mov_b32 s21, 0x1d000000
	s_mov_b32 s24, s14
	s_branch .LBB0_51
